# A4: KV up-proj GEMM takes CU index (bx+112)&255 so its third-round tiles land on CUs that had only one Q tile; on top of v040
# baseline (speedup 1.0000x reference)
.LBB0_791:
	s_add_i32 s21, s21, 0x70
	s_and_b32 s21, s21, 0xff
	s_cmpk_gt_i32 s21, 0x20f
	v_readfirstlane_b32 s5, v1
	s_mov_b64 s[76:77], 0x2000
	s_cbranch_scc1 .LBB0_817
	s_add_u32 s36, s16, 0x1ca00300
	s_addc_u32 s50, s17, 0
	s_mov_b32 s4, 0x7fffe0
	s_add_u32 s51, s47, 0x790000
	v_and_or_b32 v2, v180, s4, v184
	s_addc_u32 s52, s48, 0
	v_or3_b32 v2, v2, v183, v182
	v_lshlrev_b32_e32 v4, 1, v181
	s_ashr_i32 s54, s21, 31
	v_lshl_add_u32 v132, v2, 9, v4
	v_and_or_b32 v2, v175, s4, v179
	s_lshr_b32 s4, s54, 29
	s_add_i32 s4, s21, s4
	s_ashr_i32 s7, s5, 6
	s_ashr_i32 s8, s4, 3
	s_and_b32 s4, s4, -8
	s_ashr_i32 s6, s5, 8
	s_lshl_b32 s53, s7, 10
	s_sub_i32 s4, s21, s4
	s_cmp_lt_i32 s4, 0
	s_movk_i32 s9, 0x43
	s_cselect_b32 s9, s9, 0x42
	s_mul_i32 s4, s4, s9
	s_add_i32 s4, s4, s8
	s_ashr_i32 s8, s4, 31
	s_lshr_b32 s8, s8, 27
	s_add_i32 s8, s4, s8
	s_ashr_i32 s9, s8, 5
	s_andn2_b32 s8, s8, 31
	s_lshl_b32 s11, s9, 3
	s_sub_i32 s10, s4, s8
	s_sub_i32 s4, 0x84, s11
	s_min_u32 s12, s4, 8
	v_cvt_f32_ubyte0_e32 v6, s12
	v_cvt_f32_i32_e32 v5, s10
	v_rcp_iflag_f32_e32 v7, v6
	v_or3_b32 v2, v2, v178, v177
	v_lshlrev_b32_e32 v4, 1, v176
	v_lshl_add_u32 v2, v2, 9, v4
	v_mul_f32_e32 v4, v5, v7
	v_trunc_f32_e32 v4, v4
	v_fma_f32 v5, -v4, v6, v5
	v_cvt_i32_f32_e32 v4, v4
	s_ashr_i32 s4, s10, 30
	s_or_b32 s4, s4, 1
	v_cmp_ge_f32_e64 s[8:9], |v5|, v6
	s_and_b64 s[8:9], s[8:9], exec
	s_cselect_b32 s4, s4, 0
	v_readfirstlane_b32 s8, v4
	s_add_i32 s4, s8, s4
	s_mul_i32 s8, s4, s12
	s_sub_i32 s8, s10, s8
	s_sext_i32_i8 s8, s8
	s_add_i32 s70, s11, s8
	s_bfe_i64 s[8:9], s[4:5], 0x80000
	s_lshl_b64 s[8:9], s[8:9], 17
	s_add_u32 s26, s51, s8
	s_addc_u32 s27, s52, s9
	s_add_i32 s14, s53, 0
	s_add_i32 m0, s14, 0x10000
	s_mul_i32 s11, s70, 0x1c0000
	global_load_lds_dwordx4 v2, s[26:27]
	s_add_i32 m0, s14, 0x12000
	s_add_u32 s8, s26, 0x10000
	global_load_lds_dwordx4 v132, s[26:27]
	s_addc_u32 s9, s27, 0
	s_add_i32 m0, s14, 0x14000
	s_mul_hi_i32 s10, s70, 0x1c0000
	global_load_lds_dwordx4 v2, s[8:9]
	s_add_i32 m0, s14, 0x16000
	s_add_u32 s34, s36, s11
	s_addc_u32 s35, s50, s10
	s_add_i32 s60, s14, 0x2000
	global_load_lds_dwordx4 v132, s[8:9]
	s_mov_b32 m0, s14
	s_add_u32 s8, s34, 0xe0000
	global_load_lds_dwordx4 v154, s[34:35]
	s_mov_b32 m0, s60
	s_addc_u32 s9, s35, 0
	s_add_i32 s61, s14, 0x4000
	global_load_lds_dwordx4 v156, s[34:35]
	s_mov_b32 m0, s61
	s_add_i32 s62, s14, 0x6000
	global_load_lds_dwordx4 v154, s[8:9]
	s_mov_b32 m0, s62
	v_mov_b32_e32 v133, v3
	global_load_lds_dwordx4 v156, s[8:9]
	v_mov_b32_e32 v155, v3
	v_mov_b32_e32 v157, v3
	s_cmp_eq_u32 s6, 1
	v_lshl_add_u64 v[10:11], s[26:27], 0, v[2:3]
	v_lshl_add_u64 v[8:9], s[26:27], 0, v[132:133]
	v_lshl_add_u64 v[4:5], s[34:35], 0, v[154:155]
	s_cselect_b64 s[8:9], -1, 0
	s_cmp_lg_u32 s6, 1
	v_lshl_add_u64 v[6:7], s[34:35], 0, v[156:157]
	s_cbranch_scc1 .LBB0_794
	s_barrier
